# merge / MoBA-merge row loops: double-buffer waits no longer drain the two write-through stores issued just before them (vmcnt +2 in steady state, first pass unchanged)
# speedup vs baseline: 1.0018x; 1.0018x over previous
.LBB0_329:
	s_cmp_le_i32 s74, s2
	s_cselect_b64 s[2:3], -1, 0
	s_and_b64 s[0:1], s[2:3], s[0:1]
	s_andn2_b64 vcc, exec, s[0:1]
	s_cbranch_vccnz .LBB0_334
	v_readlane_b32 s0, v254, 41
	s_nop 1
	v_mov_b32_e32 v0, s0
	s_waitcnt vmcnt(0)
	ds_read_b64 v[2:3], v0
	v_readlane_b32 s0, v253, 0
	v_mbcnt_lo_u32_b32 v0, -1, 0
	v_mbcnt_hi_u32_b32 v0, -1, v0
	s_waitcnt lgkmcnt(0)
	v_readfirstlane_b32 s2, v2
	v_add_u32_e32 v4, s0, v0
	v_readlane_b32 s0, v253, 62
	v_readlane_b32 s1, v253, 63
	v_ashrrev_i32_e32 v5, 31, v4
	v_readfirstlane_b32 s3, v3
	v_lshl_add_u64 v[2:3], s[0:1], 0, v[4:5]
	s_mov_b64 s[0:1], 0x200000
	v_cmp_gt_u64_e32 vcc, s[0:1], v[2:3]
	s_and_saveexec_b64 s[0:1], vcc
	s_cbranch_execz .LBB0_333
	v_readlane_b32 s8, v253, 3
	v_readlane_b32 s9, v253, 4
	s_load_dword s26, s[8:9], 0x0
	v_readlane_b32 s8, v254, 26
	v_readlane_b32 s9, v254, 27
	s_mov_b64 s[36:37], 0
	s_waitcnt lgkmcnt(0)
	s_ashr_i32 s27, s26, 31
	v_lshl_add_u64 v[4:5], v[4:5], 3, s[8:9]
	s_lshl_b64 s[8:9], s[26:27], 9
	s_add_u32 s12, s2, 0x2e060000
	s_addc_u32 s13, s3, 0
	s_add_u32 s14, s2, 0x28060000
	s_addc_u32 s15, s3, 0
	s_add_u32 s16, s2, 0x2a060000
	s_addc_u32 s17, s3, 0
	s_add_u32 s18, s2, 0x2c060000
	s_addc_u32 s19, s3, 0
	s_add_u32 s30, s2, 0x26060000
	s_addc_u32 s31, s3, 0
	s_lshl_b64 s[34:35], s[26:27], 12
	s_add_u32 s38, s12, 0x100000
	s_addc_u32 s39, s13, 0
	s_add_u32 s40, s12, 0x200000
	s_addc_u32 s41, s13, 0
	s_lshl_b32 s42, s26, 9
	s_mov_b32 s43, 0x1fffff
	s_lshl_b32 s45, s42, 1
	s_mul_i32 s46, s42, 3
	s_lshl_b32 s47, s42, 2
	v_readfirstlane_b32 s44, v2
	v_min_u32_e32 v35, s43, v2
	v_lshrrev_b32_e32 v6, 1, v35
	v_lshlrev_b32_e32 v7, 4, v35
	v_and_b32_e32 v6, -4, v6
	global_load_dwordx4 v[36:39], v7, s[14:15]
	global_load_dwordx4 v[40:43], v7, s[16:17]
	global_load_dwordx4 v[44:47], v7, s[18:19]
	global_load_dword v32, v6, s[12:13]
	global_load_dword v33, v6, s[38:39]
	global_load_dword v34, v6, s[40:41]
	v_add_u32_e32 v51, s42, v2
	v_min_u32_e32 v51, s43, v51
	v_lshrrev_b32_e32 v6, 1, v51
	v_lshlrev_b32_e32 v7, 4, v51
	v_and_b32_e32 v6, -4, v6
	global_load_dwordx4 v[52:55], v7, s[14:15]
	global_load_dwordx4 v[56:59], v7, s[16:17]
	global_load_dwordx4 v[60:63], v7, s[18:19]
	global_load_dword v48, v6, s[12:13]
	global_load_dword v49, v6, s[38:39]
	global_load_dword v50, v6, s[40:41]
	s_mov_b32 s50, 0
.Lmg1_loop:
	v_add_u32_e32 v193, s45, v2
	v_min_u32_e32 v193, s43, v193
	v_lshrrev_b32_e32 v6, 1, v193
	v_lshlrev_b32_e32 v7, 4, v193
	v_and_b32_e32 v6, -4, v6
	global_load_dwordx4 v[194:197], v7, s[14:15]
	global_load_dwordx4 v[198:201], v7, s[16:17]
	global_load_dwordx4 v[202:205], v7, s[18:19]
	global_load_dword v190, v6, s[12:13]
	global_load_dword v191, v6, s[38:39]
	global_load_dword v192, v6, s[40:41]
	v_add_u32_e32 v209, s46, v2
	v_min_u32_e32 v209, s43, v209
	v_lshrrev_b32_e32 v6, 1, v209
	v_lshlrev_b32_e32 v7, 4, v209
	v_and_b32_e32 v6, -4, v6
	global_load_dwordx4 v[210:213], v7, s[14:15]
	global_load_dwordx4 v[214:217], v7, s[16:17]
	global_load_dwordx4 v[238:241], v7, s[18:19]
	global_load_dword v206, v6, s[12:13]
	global_load_dword v207, v6, s[38:39]
	global_load_dword v208, v6, s[40:41]
	s_cmp_lg_u32 s50, 0
	s_cbranch_scc1 .Lmg1_w
	s_waitcnt vmcnt(12)
.Lmg1_w:
	s_waitcnt vmcnt(14)
	s_mov_b32 s50, 1
	v_max3_f32 v8, v32, v33, v34
	v_sub_f32_e32 v9, v32, v8
	v_mul_f32_e32 v13, 0x3fb8aa3b, v9
	v_fma_f32 v14, v9, s94, -v13
	v_rndne_f32_e32 v15, v13
	v_fmac_f32_e32 v14, 0x32a5705f, v9
	v_sub_f32_e32 v13, v13, v15
	v_add_f32_e32 v13, v13, v14
	v_exp_f32_e32 v10, v13
	v_cvt_i32_f32_e32 v15, v15
	v_cmp_ngt_f32_e32 vcc, s95, v9
	v_ldexp_f32 v10, v10, v15
	s_nop 1
	v_cndmask_b32_e32 v10, 0, v10, vcc
	v_cmp_nlt_f32_e32 vcc, s96, v9
	s_nop 1
	v_cndmask_b32_e32 v10, v227, v10, vcc
	v_sub_f32_e32 v9, v33, v8
	v_mul_f32_e32 v13, 0x3fb8aa3b, v9
	v_fma_f32 v14, v9, s94, -v13
	v_rndne_f32_e32 v15, v13
	v_fmac_f32_e32 v14, 0x32a5705f, v9
	v_sub_f32_e32 v13, v13, v15
	v_add_f32_e32 v13, v13, v14
	v_exp_f32_e32 v11, v13
	v_cvt_i32_f32_e32 v15, v15
	v_cmp_ngt_f32_e32 vcc, s95, v9
	v_ldexp_f32 v11, v11, v15
	s_nop 1
	v_cndmask_b32_e32 v11, 0, v11, vcc
	v_cmp_nlt_f32_e32 vcc, s96, v9
	s_nop 1
	v_cndmask_b32_e32 v11, v227, v11, vcc
	v_sub_f32_e32 v9, v34, v8
	v_mul_f32_e32 v13, 0x3fb8aa3b, v9
	v_fma_f32 v14, v9, s94, -v13
	v_rndne_f32_e32 v15, v13
	v_fmac_f32_e32 v14, 0x32a5705f, v9
	v_sub_f32_e32 v13, v13, v15
	v_add_f32_e32 v13, v13, v14
	v_exp_f32_e32 v12, v13
	v_cvt_i32_f32_e32 v15, v15
	v_cmp_ngt_f32_e32 vcc, s95, v9
	v_ldexp_f32 v12, v12, v15
	s_nop 1
	v_cndmask_b32_e32 v12, 0, v12, vcc
	v_cmp_nlt_f32_e32 vcc, s96, v9
	s_nop 1
	v_cndmask_b32_e32 v12, v227, v12, vcc
	v_add_f32_e32 v16, v10, v11
	v_add_f32_e32 v16, v12, v16
	v_div_scale_f32 v17, s[2:3], v16, v16, 1.0
	v_rcp_f32_e32 v18, v17
	s_nop 0
	v_fma_f32 v19, -v17, v18, 1.0
	v_fmac_f32_e32 v18, v19, v18
	v_div_scale_f32 v20, vcc, 1.0, v16, 1.0
	v_mul_f32_e32 v21, v20, v18
	v_fma_f32 v22, -v17, v21, v20
	v_fmac_f32_e32 v21, v22, v18
	v_fma_f32 v17, -v17, v21, v20
	v_div_fmas_f32 v17, v17, v18, v21
	v_div_fixup_f32 v16, v17, v16, 1.0
	v_mul_f32_e32 v16, 0x41800000, v16
	v_mul_f32_e32 v10, v10, v16
	v_mul_f32_e32 v11, v11, v16
	v_mul_f32_e32 v12, v12, v16
	v_lshlrev_b32_e32 v13, 16, v36
	v_and_b32_e32 v14, 0xffff0000, v36
	v_mul_f32_e32 v20, v10, v13
	v_mul_f32_e32 v21, v10, v14
	v_lshlrev_b32_e32 v13, 16, v40
	v_and_b32_e32 v14, 0xffff0000, v40
	v_fmac_f32_e32 v20, v11, v13
	v_fmac_f32_e32 v21, v11, v14
	v_lshlrev_b32_e32 v13, 16, v44
	v_and_b32_e32 v14, 0xffff0000, v44
	v_fmac_f32_e32 v20, v12, v13
	v_fmac_f32_e32 v21, v12, v14
	v_lshlrev_b32_e32 v13, 16, v37
	v_and_b32_e32 v14, 0xffff0000, v37
	v_mul_f32_e32 v22, v10, v13
	v_mul_f32_e32 v23, v10, v14
	v_lshlrev_b32_e32 v13, 16, v41
	v_and_b32_e32 v14, 0xffff0000, v41
	v_fmac_f32_e32 v22, v11, v13
	v_fmac_f32_e32 v23, v11, v14
	v_lshlrev_b32_e32 v13, 16, v45
	v_and_b32_e32 v14, 0xffff0000, v45
	v_fmac_f32_e32 v22, v12, v13
	v_fmac_f32_e32 v23, v12, v14
	v_lshlrev_b32_e32 v13, 16, v38
	v_and_b32_e32 v14, 0xffff0000, v38
	v_mul_f32_e32 v24, v10, v13
	v_mul_f32_e32 v25, v10, v14
	v_lshlrev_b32_e32 v13, 16, v42
	v_and_b32_e32 v14, 0xffff0000, v42
	v_fmac_f32_e32 v24, v11, v13
	v_fmac_f32_e32 v25, v11, v14
	v_lshlrev_b32_e32 v13, 16, v46
	v_and_b32_e32 v14, 0xffff0000, v46
	v_fmac_f32_e32 v24, v12, v13
	v_fmac_f32_e32 v25, v12, v14
	v_lshlrev_b32_e32 v13, 16, v39
	v_and_b32_e32 v14, 0xffff0000, v39
	v_mul_f32_e32 v26, v10, v13
	v_mul_f32_e32 v27, v10, v14
	v_lshlrev_b32_e32 v13, 16, v43
	v_and_b32_e32 v14, 0xffff0000, v43
	v_fmac_f32_e32 v26, v11, v13
	v_fmac_f32_e32 v27, v11, v14
	v_lshlrev_b32_e32 v13, 16, v47
	v_and_b32_e32 v14, 0xffff0000, v47
	v_fmac_f32_e32 v26, v12, v13
	v_fmac_f32_e32 v27, v12, v14
	v_mov_b32_e32 v16, 0
	v_mov_b32_e32 v17, 0
	v_lshlrev_b32_e32 v7, 3, v35
	v_cvt_pk_fp8_f32 v16, v20, v21
	v_cvt_pk_fp8_f32 v17, v24, v25
	s_nop 0
	v_cvt_pk_fp8_f32 v16, v22, v23 op_sel:[0,0,1]
	v_cvt_pk_fp8_f32 v17, v26, v27 op_sel:[0,0,1]
	s_nop 0
	global_store_dwordx2 v7, v[16:17], s[30:31] sc0 sc1
	v_max3_f32 v8, v48, v49, v50
	v_sub_f32_e32 v9, v48, v8
	v_mul_f32_e32 v13, 0x3fb8aa3b, v9
	v_fma_f32 v14, v9, s94, -v13
	v_rndne_f32_e32 v15, v13
	v_fmac_f32_e32 v14, 0x32a5705f, v9
	v_sub_f32_e32 v13, v13, v15
	v_add_f32_e32 v13, v13, v14
	v_exp_f32_e32 v10, v13
	v_cvt_i32_f32_e32 v15, v15
	v_cmp_ngt_f32_e32 vcc, s95, v9
	v_ldexp_f32 v10, v10, v15
	s_nop 1
	v_cndmask_b32_e32 v10, 0, v10, vcc
	v_cmp_nlt_f32_e32 vcc, s96, v9
	s_nop 1
	v_cndmask_b32_e32 v10, v227, v10, vcc
	v_sub_f32_e32 v9, v49, v8
	v_mul_f32_e32 v13, 0x3fb8aa3b, v9
	v_fma_f32 v14, v9, s94, -v13
	v_rndne_f32_e32 v15, v13
	v_fmac_f32_e32 v14, 0x32a5705f, v9
	v_sub_f32_e32 v13, v13, v15
	v_add_f32_e32 v13, v13, v14
	v_exp_f32_e32 v11, v13
	v_cvt_i32_f32_e32 v15, v15
	v_cmp_ngt_f32_e32 vcc, s95, v9
	v_ldexp_f32 v11, v11, v15
	s_nop 1
	v_cndmask_b32_e32 v11, 0, v11, vcc
	v_cmp_nlt_f32_e32 vcc, s96, v9
	s_nop 1
	v_cndmask_b32_e32 v11, v227, v11, vcc
	v_sub_f32_e32 v9, v50, v8
	v_mul_f32_e32 v13, 0x3fb8aa3b, v9
	v_fma_f32 v14, v9, s94, -v13
	v_rndne_f32_e32 v15, v13
	v_fmac_f32_e32 v14, 0x32a5705f, v9
	v_sub_f32_e32 v13, v13, v15
	v_add_f32_e32 v13, v13, v14
	v_exp_f32_e32 v12, v13
	v_cvt_i32_f32_e32 v15, v15
	v_cmp_ngt_f32_e32 vcc, s95, v9
	v_ldexp_f32 v12, v12, v15
	s_nop 1
	v_cndmask_b32_e32 v12, 0, v12, vcc
	v_cmp_nlt_f32_e32 vcc, s96, v9
	s_nop 1
	v_cndmask_b32_e32 v12, v227, v12, vcc
	v_add_f32_e32 v16, v10, v11
	v_add_f32_e32 v16, v12, v16
	v_div_scale_f32 v17, s[2:3], v16, v16, 1.0
	v_rcp_f32_e32 v18, v17
	s_nop 0
	v_fma_f32 v19, -v17, v18, 1.0
	v_fmac_f32_e32 v18, v19, v18
	v_div_scale_f32 v20, vcc, 1.0, v16, 1.0
	v_mul_f32_e32 v21, v20, v18
	v_fma_f32 v22, -v17, v21, v20
	v_fmac_f32_e32 v21, v22, v18
	v_fma_f32 v17, -v17, v21, v20
	v_div_fmas_f32 v17, v17, v18, v21
	v_div_fixup_f32 v16, v17, v16, 1.0
	v_mul_f32_e32 v16, 0x41800000, v16
	v_mul_f32_e32 v10, v10, v16
	v_mul_f32_e32 v11, v11, v16
	v_mul_f32_e32 v12, v12, v16
	v_lshlrev_b32_e32 v13, 16, v52
	v_and_b32_e32 v14, 0xffff0000, v52
	v_mul_f32_e32 v20, v10, v13
	v_mul_f32_e32 v21, v10, v14
	v_lshlrev_b32_e32 v13, 16, v56
	v_and_b32_e32 v14, 0xffff0000, v56
	v_fmac_f32_e32 v20, v11, v13
	v_fmac_f32_e32 v21, v11, v14
	v_lshlrev_b32_e32 v13, 16, v60
	v_and_b32_e32 v14, 0xffff0000, v60
	v_fmac_f32_e32 v20, v12, v13
	v_fmac_f32_e32 v21, v12, v14
	v_lshlrev_b32_e32 v13, 16, v53
	v_and_b32_e32 v14, 0xffff0000, v53
	v_mul_f32_e32 v22, v10, v13
	v_mul_f32_e32 v23, v10, v14
	v_lshlrev_b32_e32 v13, 16, v57
	v_and_b32_e32 v14, 0xffff0000, v57
	v_fmac_f32_e32 v22, v11, v13
	v_fmac_f32_e32 v23, v11, v14
	v_lshlrev_b32_e32 v13, 16, v61
	v_and_b32_e32 v14, 0xffff0000, v61
	v_fmac_f32_e32 v22, v12, v13
	v_fmac_f32_e32 v23, v12, v14
	v_lshlrev_b32_e32 v13, 16, v54
	v_and_b32_e32 v14, 0xffff0000, v54
	v_mul_f32_e32 v24, v10, v13
	v_mul_f32_e32 v25, v10, v14
	v_lshlrev_b32_e32 v13, 16, v58
	v_and_b32_e32 v14, 0xffff0000, v58
	v_fmac_f32_e32 v24, v11, v13
	v_fmac_f32_e32 v25, v11, v14
	v_lshlrev_b32_e32 v13, 16, v62
	v_and_b32_e32 v14, 0xffff0000, v62
	v_fmac_f32_e32 v24, v12, v13
	v_fmac_f32_e32 v25, v12, v14
	v_lshlrev_b32_e32 v13, 16, v55
	v_and_b32_e32 v14, 0xffff0000, v55
	v_mul_f32_e32 v26, v10, v13
	v_mul_f32_e32 v27, v10, v14
	v_lshlrev_b32_e32 v13, 16, v59
	v_and_b32_e32 v14, 0xffff0000, v59
	v_fmac_f32_e32 v26, v11, v13
	v_fmac_f32_e32 v27, v11, v14
	v_lshlrev_b32_e32 v13, 16, v63
	v_and_b32_e32 v14, 0xffff0000, v63
	v_fmac_f32_e32 v26, v12, v13
	v_fmac_f32_e32 v27, v12, v14
	v_mov_b32_e32 v16, 0
	v_mov_b32_e32 v17, 0
	v_lshlrev_b32_e32 v7, 3, v51
	v_cvt_pk_fp8_f32 v16, v20, v21
	v_cvt_pk_fp8_f32 v17, v24, v25
	s_nop 0
	v_cvt_pk_fp8_f32 v16, v22, v23 op_sel:[0,0,1]
	v_cvt_pk_fp8_f32 v17, v26, v27 op_sel:[0,0,1]
	s_nop 0
	global_store_dwordx2 v7, v[16:17], s[30:31] sc0 sc1
	v_add_u32_e32 v2, s47, v2
	s_add_u32 s44, s44, s47
	v_min_u32_e32 v35, s43, v2
	v_lshrrev_b32_e32 v6, 1, v35
	v_lshlrev_b32_e32 v7, 4, v35
	v_and_b32_e32 v6, -4, v6
	global_load_dwordx4 v[36:39], v7, s[14:15]
	global_load_dwordx4 v[40:43], v7, s[16:17]
	global_load_dwordx4 v[44:47], v7, s[18:19]
	global_load_dword v32, v6, s[12:13]
	global_load_dword v33, v6, s[38:39]
	global_load_dword v34, v6, s[40:41]
	v_add_u32_e32 v51, s42, v2
	v_min_u32_e32 v51, s43, v51
	v_lshrrev_b32_e32 v6, 1, v51
	v_lshlrev_b32_e32 v7, 4, v51
	v_and_b32_e32 v6, -4, v6
	global_load_dwordx4 v[52:55], v7, s[14:15]
	global_load_dwordx4 v[56:59], v7, s[16:17]
	global_load_dwordx4 v[60:63], v7, s[18:19]
	global_load_dword v48, v6, s[12:13]
	global_load_dword v49, v6, s[38:39]
	global_load_dword v50, v6, s[40:41]
	s_waitcnt vmcnt(14)
	v_max3_f32 v8, v190, v191, v192
	v_sub_f32_e32 v9, v190, v8
	v_mul_f32_e32 v13, 0x3fb8aa3b, v9
	v_fma_f32 v14, v9, s94, -v13
	v_rndne_f32_e32 v15, v13
	v_fmac_f32_e32 v14, 0x32a5705f, v9
	v_sub_f32_e32 v13, v13, v15
	v_add_f32_e32 v13, v13, v14
	v_exp_f32_e32 v10, v13
	v_cvt_i32_f32_e32 v15, v15
	v_cmp_ngt_f32_e32 vcc, s95, v9
	v_ldexp_f32 v10, v10, v15
	s_nop 1
	v_cndmask_b32_e32 v10, 0, v10, vcc
	v_cmp_nlt_f32_e32 vcc, s96, v9
	s_nop 1
	v_cndmask_b32_e32 v10, v227, v10, vcc
	v_sub_f32_e32 v9, v191, v8
	v_mul_f32_e32 v13, 0x3fb8aa3b, v9
	v_fma_f32 v14, v9, s94, -v13
	v_rndne_f32_e32 v15, v13
	v_fmac_f32_e32 v14, 0x32a5705f, v9
	v_sub_f32_e32 v13, v13, v15
	v_add_f32_e32 v13, v13, v14
	v_exp_f32_e32 v11, v13
	v_cvt_i32_f32_e32 v15, v15
	v_cmp_ngt_f32_e32 vcc, s95, v9
	v_ldexp_f32 v11, v11, v15
	s_nop 1
	v_cndmask_b32_e32 v11, 0, v11, vcc
	v_cmp_nlt_f32_e32 vcc, s96, v9
	s_nop 1
	v_cndmask_b32_e32 v11, v227, v11, vcc
	v_sub_f32_e32 v9, v192, v8
	v_mul_f32_e32 v13, 0x3fb8aa3b, v9
	v_fma_f32 v14, v9, s94, -v13
	v_rndne_f32_e32 v15, v13
	v_fmac_f32_e32 v14, 0x32a5705f, v9
	v_sub_f32_e32 v13, v13, v15
	v_add_f32_e32 v13, v13, v14
	v_exp_f32_e32 v12, v13
	v_cvt_i32_f32_e32 v15, v15
	v_cmp_ngt_f32_e32 vcc, s95, v9
	v_ldexp_f32 v12, v12, v15
	s_nop 1
	v_cndmask_b32_e32 v12, 0, v12, vcc
	v_cmp_nlt_f32_e32 vcc, s96, v9
	s_nop 1
	v_cndmask_b32_e32 v12, v227, v12, vcc
	v_add_f32_e32 v16, v10, v11
	v_add_f32_e32 v16, v12, v16
	v_div_scale_f32 v17, s[2:3], v16, v16, 1.0
	v_rcp_f32_e32 v18, v17
	s_nop 0
	v_fma_f32 v19, -v17, v18, 1.0
	v_fmac_f32_e32 v18, v19, v18
	v_div_scale_f32 v20, vcc, 1.0, v16, 1.0
	v_mul_f32_e32 v21, v20, v18
	v_fma_f32 v22, -v17, v21, v20
	v_fmac_f32_e32 v21, v22, v18
	v_fma_f32 v17, -v17, v21, v20
	v_div_fmas_f32 v17, v17, v18, v21
	v_div_fixup_f32 v16, v17, v16, 1.0
	v_mul_f32_e32 v16, 0x41800000, v16
	v_mul_f32_e32 v10, v10, v16
	v_mul_f32_e32 v11, v11, v16
	v_mul_f32_e32 v12, v12, v16
	v_lshlrev_b32_e32 v13, 16, v194
	v_and_b32_e32 v14, 0xffff0000, v194
	v_mul_f32_e32 v20, v10, v13
	v_mul_f32_e32 v21, v10, v14
	v_lshlrev_b32_e32 v13, 16, v198
	v_and_b32_e32 v14, 0xffff0000, v198
	v_fmac_f32_e32 v20, v11, v13
	v_fmac_f32_e32 v21, v11, v14
	v_lshlrev_b32_e32 v13, 16, v202
	v_and_b32_e32 v14, 0xffff0000, v202
	v_fmac_f32_e32 v20, v12, v13
	v_fmac_f32_e32 v21, v12, v14
	v_lshlrev_b32_e32 v13, 16, v195
	v_and_b32_e32 v14, 0xffff0000, v195
	v_mul_f32_e32 v22, v10, v13
	v_mul_f32_e32 v23, v10, v14
	v_lshlrev_b32_e32 v13, 16, v199
	v_and_b32_e32 v14, 0xffff0000, v199
	v_fmac_f32_e32 v22, v11, v13
	v_fmac_f32_e32 v23, v11, v14
	v_lshlrev_b32_e32 v13, 16, v203
	v_and_b32_e32 v14, 0xffff0000, v203
	v_fmac_f32_e32 v22, v12, v13
	v_fmac_f32_e32 v23, v12, v14
	v_lshlrev_b32_e32 v13, 16, v196
	v_and_b32_e32 v14, 0xffff0000, v196
	v_mul_f32_e32 v24, v10, v13
	v_mul_f32_e32 v25, v10, v14
	v_lshlrev_b32_e32 v13, 16, v200
	v_and_b32_e32 v14, 0xffff0000, v200
	v_fmac_f32_e32 v24, v11, v13
	v_fmac_f32_e32 v25, v11, v14
	v_lshlrev_b32_e32 v13, 16, v204
	v_and_b32_e32 v14, 0xffff0000, v204
	v_fmac_f32_e32 v24, v12, v13
	v_fmac_f32_e32 v25, v12, v14
	v_lshlrev_b32_e32 v13, 16, v197
	v_and_b32_e32 v14, 0xffff0000, v197
	v_mul_f32_e32 v26, v10, v13
	v_mul_f32_e32 v27, v10, v14
	v_lshlrev_b32_e32 v13, 16, v201
	v_and_b32_e32 v14, 0xffff0000, v201
	v_fmac_f32_e32 v26, v11, v13
	v_fmac_f32_e32 v27, v11, v14
	v_lshlrev_b32_e32 v13, 16, v205
	v_and_b32_e32 v14, 0xffff0000, v205
	v_fmac_f32_e32 v26, v12, v13
	v_fmac_f32_e32 v27, v12, v14
	v_mov_b32_e32 v16, 0
	v_mov_b32_e32 v17, 0
	v_lshlrev_b32_e32 v7, 3, v193
	v_cvt_pk_fp8_f32 v16, v20, v21
	v_cvt_pk_fp8_f32 v17, v24, v25
	s_nop 0
	v_cvt_pk_fp8_f32 v16, v22, v23 op_sel:[0,0,1]
	v_cvt_pk_fp8_f32 v17, v26, v27 op_sel:[0,0,1]
	s_nop 0
	global_store_dwordx2 v7, v[16:17], s[30:31] sc0 sc1
	v_max3_f32 v8, v206, v207, v208
	v_sub_f32_e32 v9, v206, v8
	v_mul_f32_e32 v13, 0x3fb8aa3b, v9
	v_fma_f32 v14, v9, s94, -v13
	v_rndne_f32_e32 v15, v13
	v_fmac_f32_e32 v14, 0x32a5705f, v9
	v_sub_f32_e32 v13, v13, v15
	v_add_f32_e32 v13, v13, v14
	v_exp_f32_e32 v10, v13
	v_cvt_i32_f32_e32 v15, v15
	v_cmp_ngt_f32_e32 vcc, s95, v9
	v_ldexp_f32 v10, v10, v15
	s_nop 1
	v_cndmask_b32_e32 v10, 0, v10, vcc
	v_cmp_nlt_f32_e32 vcc, s96, v9
	s_nop 1
	v_cndmask_b32_e32 v10, v227, v10, vcc
	v_sub_f32_e32 v9, v207, v8
	v_mul_f32_e32 v13, 0x3fb8aa3b, v9
	v_fma_f32 v14, v9, s94, -v13
	v_rndne_f32_e32 v15, v13
	v_fmac_f32_e32 v14, 0x32a5705f, v9
	v_sub_f32_e32 v13, v13, v15
	v_add_f32_e32 v13, v13, v14
	v_exp_f32_e32 v11, v13
	v_cvt_i32_f32_e32 v15, v15
	v_cmp_ngt_f32_e32 vcc, s95, v9
	v_ldexp_f32 v11, v11, v15
	s_nop 1
	v_cndmask_b32_e32 v11, 0, v11, vcc
	v_cmp_nlt_f32_e32 vcc, s96, v9
	s_nop 1
	v_cndmask_b32_e32 v11, v227, v11, vcc
	v_sub_f32_e32 v9, v208, v8
	v_mul_f32_e32 v13, 0x3fb8aa3b, v9
	v_fma_f32 v14, v9, s94, -v13
	v_rndne_f32_e32 v15, v13
	v_fmac_f32_e32 v14, 0x32a5705f, v9
	v_sub_f32_e32 v13, v13, v15
	v_add_f32_e32 v13, v13, v14
	v_exp_f32_e32 v12, v13
	v_cvt_i32_f32_e32 v15, v15
	v_cmp_ngt_f32_e32 vcc, s95, v9
	v_ldexp_f32 v12, v12, v15
	s_nop 1
	v_cndmask_b32_e32 v12, 0, v12, vcc
	v_cmp_nlt_f32_e32 vcc, s96, v9
	s_nop 1
	v_cndmask_b32_e32 v12, v227, v12, vcc
	v_add_f32_e32 v16, v10, v11
	v_add_f32_e32 v16, v12, v16
	v_div_scale_f32 v17, s[2:3], v16, v16, 1.0
	v_rcp_f32_e32 v18, v17
	s_nop 0
	v_fma_f32 v19, -v17, v18, 1.0
	v_fmac_f32_e32 v18, v19, v18
	v_div_scale_f32 v20, vcc, 1.0, v16, 1.0
	v_mul_f32_e32 v21, v20, v18
	v_fma_f32 v22, -v17, v21, v20
	v_fmac_f32_e32 v21, v22, v18
	v_fma_f32 v17, -v17, v21, v20
	v_div_fmas_f32 v17, v17, v18, v21
	v_div_fixup_f32 v16, v17, v16, 1.0
	v_mul_f32_e32 v16, 0x41800000, v16
	v_mul_f32_e32 v10, v10, v16
	v_mul_f32_e32 v11, v11, v16
	v_mul_f32_e32 v12, v12, v16
	v_lshlrev_b32_e32 v13, 16, v210
	v_and_b32_e32 v14, 0xffff0000, v210
	v_mul_f32_e32 v20, v10, v13
	v_mul_f32_e32 v21, v10, v14
	v_lshlrev_b32_e32 v13, 16, v214
	v_and_b32_e32 v14, 0xffff0000, v214
	v_fmac_f32_e32 v20, v11, v13
	v_fmac_f32_e32 v21, v11, v14
	v_lshlrev_b32_e32 v13, 16, v238
	v_and_b32_e32 v14, 0xffff0000, v238
	v_fmac_f32_e32 v20, v12, v13
	v_fmac_f32_e32 v21, v12, v14
	v_lshlrev_b32_e32 v13, 16, v211
	v_and_b32_e32 v14, 0xffff0000, v211
	v_mul_f32_e32 v22, v10, v13
	v_mul_f32_e32 v23, v10, v14
	v_lshlrev_b32_e32 v13, 16, v215
	v_and_b32_e32 v14, 0xffff0000, v215
	v_fmac_f32_e32 v22, v11, v13
	v_fmac_f32_e32 v23, v11, v14
	v_lshlrev_b32_e32 v13, 16, v239
	v_and_b32_e32 v14, 0xffff0000, v239
	v_fmac_f32_e32 v22, v12, v13
	v_fmac_f32_e32 v23, v12, v14
	v_lshlrev_b32_e32 v13, 16, v212
	v_and_b32_e32 v14, 0xffff0000, v212
	v_mul_f32_e32 v24, v10, v13
	v_mul_f32_e32 v25, v10, v14
	v_lshlrev_b32_e32 v13, 16, v216
	v_and_b32_e32 v14, 0xffff0000, v216
	v_fmac_f32_e32 v24, v11, v13
	v_fmac_f32_e32 v25, v11, v14
	v_lshlrev_b32_e32 v13, 16, v240
	v_and_b32_e32 v14, 0xffff0000, v240
	v_fmac_f32_e32 v24, v12, v13
	v_fmac_f32_e32 v25, v12, v14
	v_lshlrev_b32_e32 v13, 16, v213
	v_and_b32_e32 v14, 0xffff0000, v213
	v_mul_f32_e32 v26, v10, v13
	v_mul_f32_e32 v27, v10, v14
	v_lshlrev_b32_e32 v13, 16, v217
	v_and_b32_e32 v14, 0xffff0000, v217
	v_fmac_f32_e32 v26, v11, v13
	v_fmac_f32_e32 v27, v11, v14
	v_lshlrev_b32_e32 v13, 16, v241
	v_and_b32_e32 v14, 0xffff0000, v241
	v_fmac_f32_e32 v26, v12, v13
	v_fmac_f32_e32 v27, v12, v14
	v_mov_b32_e32 v16, 0
	v_mov_b32_e32 v17, 0
	v_lshlrev_b32_e32 v7, 3, v209
	v_cvt_pk_fp8_f32 v16, v20, v21
	v_cvt_pk_fp8_f32 v17, v24, v25
	s_nop 0
	v_cvt_pk_fp8_f32 v16, v22, v23 op_sel:[0,0,1]
	v_cvt_pk_fp8_f32 v17, v26, v27 op_sel:[0,0,1]
	s_nop 0
	global_store_dwordx2 v7, v[16:17], s[30:31] sc0 sc1
	s_cmp_le_u32 s44, s43
	s_cbranch_scc1 .Lmg1_loop

.LBB0_875:
	v_readlane_b32 s0, v254, 10
	v_readlane_b32 s1, v254, 11
	s_andn2_b64 vcc, exec, s[0:1]
	s_cbranch_vccnz .LBB0_894
	v_readlane_b32 s0, v254, 41
	v_readlane_b32 s2, v253, 62
	v_readlane_b32 s3, v253, 63
	v_mov_b32_e32 v0, s0
	s_waitcnt vmcnt(0)
	ds_read_b64 v[2:3], v0
	v_readlane_b32 s0, v253, 0
	v_mbcnt_lo_u32_b32 v0, -1, 0
	v_mbcnt_hi_u32_b32 v0, -1, v0
	s_waitcnt lgkmcnt(0)
	v_readfirstlane_b32 s1, v3
	v_add_u32_e32 v4, s0, v0
	v_readfirstlane_b32 s0, v2
	v_ashrrev_i32_e32 v5, 31, v4
	v_lshl_add_u64 v[2:3], s[2:3], 0, v[4:5]
	s_mov_b64 s[2:3], 0x200000
	v_cmp_gt_u64_e32 vcc, s[2:3], v[2:3]
	s_and_saveexec_b64 s[8:9], vcc
	s_cbranch_execz .LBB0_893
	v_readlane_b32 s2, v253, 3
	v_readlane_b32 s3, v253, 4
	s_load_dword s2, s[2:3], 0x0
	v_lshlrev_b32_e32 v0, 3, v4
	v_and_b32_e32 v4, 56, v0
	v_lshlrev_b32_e32 v0, 1, v4
	v_lshl_add_u64 v[6:7], s[0:1], 0, v[0:1]
	s_waitcnt lgkmcnt(0)
	s_ashr_i32 s3, s2, 31
	s_lshl_b64 s[12:13], s[2:3], 9
	s_add_u32 s14, s0, 0x4dce0a00
	s_addc_u32 s15, s1, 0
	s_add_u32 s16, s0, 0x26060000
	s_addc_u32 s17, s1, 0
	s_mov_b64 s[0:1], 0x45ce0a00
	v_mov_b32_e32 v5, v1
	v_lshl_add_u64 v[6:7], v[6:7], 0, s[0:1]
	s_mov_b64 s[18:19], 0
	s_sub_u32 s44, s14, 0x8000000
	s_subb_u32 s45, s15, 0
	s_mov_b32 s42, s12
	s_mov_b32 s43, 0x1fffff
	s_lshl_b32 s46, s42, 1
	s_mul_i32 s47, s42, 3
	s_lshl_b32 s48, s42, 2
	v_mov_b32_e32 v148, 0
	v_mov_b32_e32 v64, 0x80
	v_mov_b32_e32 v65, 0x100
	v_mov_b32_e32 v149, 0xff800000
	v_mov_b32_e32 v150, 0x180
	v_readfirstlane_b32 s49, v2
	v_min_u32_e32 v190, s43, v2
	v_lshrrev_b32_e32 v9, 3, v190
	v_bfe_u32 v8, v190, 15, 5
	v_and_b32_e32 v10, 7, v190
	v_lshlrev_b32_e32 v11, 9, v9
	v_lshlrev_b32_e32 v9, 4, v9
	v_lshl_add_u32 v10, v10, 4, v11
	global_load_dwordx4 v[32:35], v9, s[14:15]
	global_load_dwordx4 v[48:51], v10, s[44:45] offset:384
	v_cmp_lt_u32_e32 vcc, 0, v8
	s_nop 1
	v_cndmask_b32_e32 v11, v150, v148, vcc
	v_add_u32_e32 v11, v11, v10
	global_load_dwordx4 v[36:39], v11, s[44:45]
	v_cmp_lt_u32_e32 vcc, 1, v8
	s_nop 1
	v_cndmask_b32_e32 v11, v150, v64, vcc
	v_add_u32_e32 v11, v11, v10
	global_load_dwordx4 v[40:43], v11, s[44:45]
	v_cmp_lt_u32_e32 vcc, 2, v8
	s_nop 1
	v_cndmask_b32_e32 v11, v150, v65, vcc
	v_add_u32_e32 v11, v11, v10
	global_load_dwordx4 v[44:47], v11, s[44:45]
	v_add_u32_e32 v191, s42, v2
	v_min_u32_e32 v191, s43, v191
	v_lshrrev_b32_e32 v9, 3, v191
	v_bfe_u32 v8, v191, 15, 5
	v_and_b32_e32 v10, 7, v191
	v_lshlrev_b32_e32 v11, 9, v9
	v_lshlrev_b32_e32 v9, 4, v9
	v_lshl_add_u32 v10, v10, 4, v11
	global_load_dwordx4 v[52:55], v9, s[14:15]
	global_load_dwordx4 v[196:199], v10, s[44:45] offset:384
	v_cmp_lt_u32_e32 vcc, 0, v8
	s_nop 1
	v_cndmask_b32_e32 v11, v150, v148, vcc
	v_add_u32_e32 v11, v11, v10
	global_load_dwordx4 v[56:59], v11, s[44:45]
	v_cmp_lt_u32_e32 vcc, 1, v8
	s_nop 1
	v_cndmask_b32_e32 v11, v150, v64, vcc
	v_add_u32_e32 v11, v11, v10
	global_load_dwordx4 v[60:63], v11, s[44:45]
	v_cmp_lt_u32_e32 vcc, 2, v8
	s_nop 1
	v_cndmask_b32_e32 v11, v150, v65, vcc
	v_add_u32_e32 v11, v11, v10
	global_load_dwordx4 v[192:195], v11, s[44:45]
	s_mov_b32 s50, 0
.Lmbm_loop:
	v_add_u32_e32 v238, s46, v2
	v_min_u32_e32 v238, s43, v238
	v_lshrrev_b32_e32 v9, 3, v238
	v_bfe_u32 v8, v238, 15, 5
	v_and_b32_e32 v10, 7, v238
	v_lshlrev_b32_e32 v11, 9, v9
	v_lshlrev_b32_e32 v9, 4, v9
	v_lshl_add_u32 v10, v10, 4, v11
	global_load_dwordx4 v[200:203], v9, s[14:15]
	global_load_dwordx4 v[216:219], v10, s[44:45] offset:384
	v_cmp_lt_u32_e32 vcc, 0, v8
	s_nop 1
	v_cndmask_b32_e32 v11, v150, v148, vcc
	v_add_u32_e32 v11, v11, v10
	global_load_dwordx4 v[204:207], v11, s[44:45]
	v_cmp_lt_u32_e32 vcc, 1, v8
	s_nop 1
	v_cndmask_b32_e32 v11, v150, v64, vcc
	v_add_u32_e32 v11, v11, v10
	global_load_dwordx4 v[208:211], v11, s[44:45]
	v_cmp_lt_u32_e32 vcc, 2, v8
	s_nop 1
	v_cndmask_b32_e32 v11, v150, v65, vcc
	v_add_u32_e32 v11, v11, v10
	global_load_dwordx4 v[212:215], v11, s[44:45]
	v_add_u32_e32 v239, s47, v2
	v_min_u32_e32 v239, s43, v239
	v_lshrrev_b32_e32 v9, 3, v239
	v_bfe_u32 v8, v239, 15, 5
	v_and_b32_e32 v10, 7, v239
	v_lshlrev_b32_e32 v11, 9, v9
	v_lshlrev_b32_e32 v9, 4, v9
	v_lshl_add_u32 v10, v10, 4, v11
	global_load_dwordx4 v[240:243], v9, s[14:15]
	global_load_dwordx4 v[136:139], v10, s[44:45] offset:384
	v_cmp_lt_u32_e32 vcc, 0, v8
	s_nop 1
	v_cndmask_b32_e32 v11, v150, v148, vcc
	v_add_u32_e32 v11, v11, v10
	global_load_dwordx4 v[244:247], v11, s[44:45]
	v_cmp_lt_u32_e32 vcc, 1, v8
	s_nop 1
	v_cndmask_b32_e32 v11, v150, v64, vcc
	v_add_u32_e32 v11, v11, v10
	global_load_dwordx4 v[248:251], v11, s[44:45]
	v_cmp_lt_u32_e32 vcc, 2, v8
	s_nop 1
	v_cndmask_b32_e32 v11, v150, v65, vcc
	v_add_u32_e32 v11, v11, v10
	global_load_dwordx4 v[124:127], v11, s[44:45]
	s_cmp_lg_u32 s50, 0
	s_cbranch_scc1 .Lmbm_w
	s_waitcnt vmcnt(10)
.Lmbm_w:
	s_waitcnt vmcnt(12)
	s_mov_b32 s50, 1
	v_bfe_u32 v8, v190, 15, 5
	v_cmp_lt_u32_e32 vcc, 0, v8
	s_nop 1
	v_cndmask_b32_e32 v32, v149, v32, vcc
	v_cmp_lt_u32_e32 vcc, 1, v8
	s_nop 1
	v_cndmask_b32_e32 v33, v149, v33, vcc
	v_cmp_lt_u32_e32 vcc, 2, v8
	s_nop 1
	v_cndmask_b32_e32 v34, v149, v34, vcc
	v_max3_f32 v9, v32, v33, v34
	v_max_f32_e32 v9, v9, v35
	v_sub_f32_e32 v10, v32, v9
	v_mul_f32_e32 v16, 0x3fb8aa3b, v10
	v_fma_f32 v17, v10, s94, -v16
	v_rndne_f32_e32 v18, v16
	v_fmac_f32_e32 v17, 0x32a5705f, v10
	v_sub_f32_e32 v16, v16, v18
	v_add_f32_e32 v16, v16, v17
	v_exp_f32_e32 v12, v16
	v_cvt_i32_f32_e32 v18, v18
	v_cmp_ngt_f32_e32 vcc, s95, v10
	v_ldexp_f32 v12, v12, v18
	s_nop 1
	v_cndmask_b32_e32 v12, 0, v12, vcc
	v_cmp_nlt_f32_e32 vcc, s96, v10
	s_nop 1
	v_cndmask_b32_e32 v12, v227, v12, vcc
	v_sub_f32_e32 v10, v33, v9
	v_mul_f32_e32 v16, 0x3fb8aa3b, v10
	v_fma_f32 v17, v10, s94, -v16
	v_rndne_f32_e32 v18, v16
	v_fmac_f32_e32 v17, 0x32a5705f, v10
	v_sub_f32_e32 v16, v16, v18
	v_add_f32_e32 v16, v16, v17
	v_exp_f32_e32 v13, v16
	v_cvt_i32_f32_e32 v18, v18
	v_cmp_ngt_f32_e32 vcc, s95, v10
	v_ldexp_f32 v13, v13, v18
	s_nop 1
	v_cndmask_b32_e32 v13, 0, v13, vcc
	v_cmp_nlt_f32_e32 vcc, s96, v10
	s_nop 1
	v_cndmask_b32_e32 v13, v227, v13, vcc
	v_sub_f32_e32 v10, v34, v9
	v_mul_f32_e32 v16, 0x3fb8aa3b, v10
	v_fma_f32 v17, v10, s94, -v16
	v_rndne_f32_e32 v18, v16
	v_fmac_f32_e32 v17, 0x32a5705f, v10
	v_sub_f32_e32 v16, v16, v18
	v_add_f32_e32 v16, v16, v17
	v_exp_f32_e32 v14, v16
	v_cvt_i32_f32_e32 v18, v18
	v_cmp_ngt_f32_e32 vcc, s95, v10
	v_ldexp_f32 v14, v14, v18
	s_nop 1
	v_cndmask_b32_e32 v14, 0, v14, vcc
	v_cmp_nlt_f32_e32 vcc, s96, v10
	s_nop 1
	v_cndmask_b32_e32 v14, v227, v14, vcc
	v_sub_f32_e32 v10, v35, v9
	v_mul_f32_e32 v16, 0x3fb8aa3b, v10
	v_fma_f32 v17, v10, s94, -v16
	v_rndne_f32_e32 v18, v16
	v_fmac_f32_e32 v17, 0x32a5705f, v10
	v_sub_f32_e32 v16, v16, v18
	v_add_f32_e32 v16, v16, v17
	v_exp_f32_e32 v15, v16
	v_cvt_i32_f32_e32 v18, v18
	v_cmp_ngt_f32_e32 vcc, s95, v10
	v_ldexp_f32 v15, v15, v18
	s_nop 1
	v_cndmask_b32_e32 v15, 0, v15, vcc
	v_cmp_nlt_f32_e32 vcc, s96, v10
	s_nop 1
	v_cndmask_b32_e32 v15, v227, v15, vcc
	v_add_f32_e32 v16, v12, v13
	v_add_f32_e32 v16, v14, v16
	v_add_f32_e32 v16, v15, v16
	v_div_scale_f32 v17, s[2:3], v16, v16, 1.0
	v_rcp_f32_e32 v18, v17
	s_nop 0
	v_fma_f32 v19, -v17, v18, 1.0
	v_fmac_f32_e32 v18, v19, v18
	v_div_scale_f32 v20, vcc, 1.0, v16, 1.0
	v_mul_f32_e32 v21, v20, v18
	v_fma_f32 v22, -v17, v21, v20
	v_fmac_f32_e32 v21, v22, v18
	v_fma_f32 v17, -v17, v21, v20
	v_div_fmas_f32 v17, v17, v18, v21
	v_div_fixup_f32 v16, v17, v16, 1.0
	v_mul_f32_e32 v16, 0x41800000, v16
	v_mul_f32_e32 v12, v12, v16
	v_mul_f32_e32 v13, v13, v16
	v_mul_f32_e32 v14, v14, v16
	v_mul_f32_e32 v15, v15, v16
	v_lshlrev_b32_e32 v16, 16, v36
	v_and_b32_e32 v17, 0xffff0000, v36
	v_mul_f32_e32 v20, v12, v16
	v_mul_f32_e32 v21, v12, v17
	v_lshlrev_b32_e32 v16, 16, v40
	v_and_b32_e32 v17, 0xffff0000, v40
	v_fmac_f32_e32 v20, v13, v16
	v_fmac_f32_e32 v21, v13, v17
	v_lshlrev_b32_e32 v16, 16, v44
	v_and_b32_e32 v17, 0xffff0000, v44
	v_fmac_f32_e32 v20, v14, v16
	v_fmac_f32_e32 v21, v14, v17
	v_lshlrev_b32_e32 v16, 16, v48
	v_and_b32_e32 v17, 0xffff0000, v48
	v_fmac_f32_e32 v20, v15, v16
	v_fmac_f32_e32 v21, v15, v17
	v_lshlrev_b32_e32 v16, 16, v37
	v_and_b32_e32 v17, 0xffff0000, v37
	v_mul_f32_e32 v22, v12, v16
	v_mul_f32_e32 v23, v12, v17
	v_lshlrev_b32_e32 v16, 16, v41
	v_and_b32_e32 v17, 0xffff0000, v41
	v_fmac_f32_e32 v22, v13, v16
	v_fmac_f32_e32 v23, v13, v17
	v_lshlrev_b32_e32 v16, 16, v45
	v_and_b32_e32 v17, 0xffff0000, v45
	v_fmac_f32_e32 v22, v14, v16
	v_fmac_f32_e32 v23, v14, v17
	v_lshlrev_b32_e32 v16, 16, v49
	v_and_b32_e32 v17, 0xffff0000, v49
	v_fmac_f32_e32 v22, v15, v16
	v_fmac_f32_e32 v23, v15, v17
	v_lshlrev_b32_e32 v16, 16, v38
	v_and_b32_e32 v17, 0xffff0000, v38
	v_mul_f32_e32 v24, v12, v16
	v_mul_f32_e32 v25, v12, v17
	v_lshlrev_b32_e32 v16, 16, v42
	v_and_b32_e32 v17, 0xffff0000, v42
	v_fmac_f32_e32 v24, v13, v16
	v_fmac_f32_e32 v25, v13, v17
	v_lshlrev_b32_e32 v16, 16, v46
	v_and_b32_e32 v17, 0xffff0000, v46
	v_fmac_f32_e32 v24, v14, v16
	v_fmac_f32_e32 v25, v14, v17
	v_lshlrev_b32_e32 v16, 16, v50
	v_and_b32_e32 v17, 0xffff0000, v50
	v_fmac_f32_e32 v24, v15, v16
	v_fmac_f32_e32 v25, v15, v17
	v_lshlrev_b32_e32 v16, 16, v39
	v_and_b32_e32 v17, 0xffff0000, v39
	v_mul_f32_e32 v26, v12, v16
	v_mul_f32_e32 v27, v12, v17
	v_lshlrev_b32_e32 v16, 16, v43
	v_and_b32_e32 v17, 0xffff0000, v43
	v_fmac_f32_e32 v26, v13, v16
	v_fmac_f32_e32 v27, v13, v17
	v_lshlrev_b32_e32 v16, 16, v47
	v_and_b32_e32 v17, 0xffff0000, v47
	v_fmac_f32_e32 v26, v14, v16
	v_fmac_f32_e32 v27, v14, v17
	v_lshlrev_b32_e32 v16, 16, v51
	v_and_b32_e32 v17, 0xffff0000, v51
	v_fmac_f32_e32 v26, v15, v16
	v_fmac_f32_e32 v27, v15, v17
	v_mov_b32_e32 v18, 0
	v_mov_b32_e32 v19, 0
	v_lshlrev_b32_e32 v11, 3, v190
	v_cvt_pk_fp8_f32 v18, v20, v21
	v_cvt_pk_fp8_f32 v19, v24, v25
	s_nop 0
	v_cvt_pk_fp8_f32 v18, v22, v23 op_sel:[0,0,1]
	v_cvt_pk_fp8_f32 v19, v26, v27 op_sel:[0,0,1]
	s_nop 0
	global_store_dwordx2 v11, v[18:19], s[16:17] sc0 sc1
	v_bfe_u32 v8, v191, 15, 5
	v_cmp_lt_u32_e32 vcc, 0, v8
	s_nop 1
	v_cndmask_b32_e32 v52, v149, v52, vcc
	v_cmp_lt_u32_e32 vcc, 1, v8
	s_nop 1
	v_cndmask_b32_e32 v53, v149, v53, vcc
	v_cmp_lt_u32_e32 vcc, 2, v8
	s_nop 1
	v_cndmask_b32_e32 v54, v149, v54, vcc
	v_max3_f32 v9, v52, v53, v54
	v_max_f32_e32 v9, v9, v55
	v_sub_f32_e32 v10, v52, v9
	v_mul_f32_e32 v16, 0x3fb8aa3b, v10
	v_fma_f32 v17, v10, s94, -v16
	v_rndne_f32_e32 v18, v16
	v_fmac_f32_e32 v17, 0x32a5705f, v10
	v_sub_f32_e32 v16, v16, v18
	v_add_f32_e32 v16, v16, v17
	v_exp_f32_e32 v12, v16
	v_cvt_i32_f32_e32 v18, v18
	v_cmp_ngt_f32_e32 vcc, s95, v10
	v_ldexp_f32 v12, v12, v18
	s_nop 1
	v_cndmask_b32_e32 v12, 0, v12, vcc
	v_cmp_nlt_f32_e32 vcc, s96, v10
	s_nop 1
	v_cndmask_b32_e32 v12, v227, v12, vcc
	v_sub_f32_e32 v10, v53, v9
	v_mul_f32_e32 v16, 0x3fb8aa3b, v10
	v_fma_f32 v17, v10, s94, -v16
	v_rndne_f32_e32 v18, v16
	v_fmac_f32_e32 v17, 0x32a5705f, v10
	v_sub_f32_e32 v16, v16, v18
	v_add_f32_e32 v16, v16, v17
	v_exp_f32_e32 v13, v16
	v_cvt_i32_f32_e32 v18, v18
	v_cmp_ngt_f32_e32 vcc, s95, v10
	v_ldexp_f32 v13, v13, v18
	s_nop 1
	v_cndmask_b32_e32 v13, 0, v13, vcc
	v_cmp_nlt_f32_e32 vcc, s96, v10
	s_nop 1
	v_cndmask_b32_e32 v13, v227, v13, vcc
	v_sub_f32_e32 v10, v54, v9
	v_mul_f32_e32 v16, 0x3fb8aa3b, v10
	v_fma_f32 v17, v10, s94, -v16
	v_rndne_f32_e32 v18, v16
	v_fmac_f32_e32 v17, 0x32a5705f, v10
	v_sub_f32_e32 v16, v16, v18
	v_add_f32_e32 v16, v16, v17
	v_exp_f32_e32 v14, v16
	v_cvt_i32_f32_e32 v18, v18
	v_cmp_ngt_f32_e32 vcc, s95, v10
	v_ldexp_f32 v14, v14, v18
	s_nop 1
	v_cndmask_b32_e32 v14, 0, v14, vcc
	v_cmp_nlt_f32_e32 vcc, s96, v10
	s_nop 1
	v_cndmask_b32_e32 v14, v227, v14, vcc
	v_sub_f32_e32 v10, v55, v9
	v_mul_f32_e32 v16, 0x3fb8aa3b, v10
	v_fma_f32 v17, v10, s94, -v16
	v_rndne_f32_e32 v18, v16
	v_fmac_f32_e32 v17, 0x32a5705f, v10
	v_sub_f32_e32 v16, v16, v18
	v_add_f32_e32 v16, v16, v17
	v_exp_f32_e32 v15, v16
	v_cvt_i32_f32_e32 v18, v18
	v_cmp_ngt_f32_e32 vcc, s95, v10
	v_ldexp_f32 v15, v15, v18
	s_nop 1
	v_cndmask_b32_e32 v15, 0, v15, vcc
	v_cmp_nlt_f32_e32 vcc, s96, v10
	s_nop 1
	v_cndmask_b32_e32 v15, v227, v15, vcc
	v_add_f32_e32 v16, v12, v13
	v_add_f32_e32 v16, v14, v16
	v_add_f32_e32 v16, v15, v16
	v_div_scale_f32 v17, s[2:3], v16, v16, 1.0
	v_rcp_f32_e32 v18, v17
	s_nop 0
	v_fma_f32 v19, -v17, v18, 1.0
	v_fmac_f32_e32 v18, v19, v18
	v_div_scale_f32 v20, vcc, 1.0, v16, 1.0
	v_mul_f32_e32 v21, v20, v18
	v_fma_f32 v22, -v17, v21, v20
	v_fmac_f32_e32 v21, v22, v18
	v_fma_f32 v17, -v17, v21, v20
	v_div_fmas_f32 v17, v17, v18, v21
	v_div_fixup_f32 v16, v17, v16, 1.0
	v_mul_f32_e32 v16, 0x41800000, v16
	v_mul_f32_e32 v12, v12, v16
	v_mul_f32_e32 v13, v13, v16
	v_mul_f32_e32 v14, v14, v16
	v_mul_f32_e32 v15, v15, v16
	v_lshlrev_b32_e32 v16, 16, v56
	v_and_b32_e32 v17, 0xffff0000, v56
	v_mul_f32_e32 v20, v12, v16
	v_mul_f32_e32 v21, v12, v17
	v_lshlrev_b32_e32 v16, 16, v60
	v_and_b32_e32 v17, 0xffff0000, v60
	v_fmac_f32_e32 v20, v13, v16
	v_fmac_f32_e32 v21, v13, v17
	v_lshlrev_b32_e32 v16, 16, v192
	v_and_b32_e32 v17, 0xffff0000, v192
	v_fmac_f32_e32 v20, v14, v16
	v_fmac_f32_e32 v21, v14, v17
	v_lshlrev_b32_e32 v16, 16, v196
	v_and_b32_e32 v17, 0xffff0000, v196
	v_fmac_f32_e32 v20, v15, v16
	v_fmac_f32_e32 v21, v15, v17
	v_lshlrev_b32_e32 v16, 16, v57
	v_and_b32_e32 v17, 0xffff0000, v57
	v_mul_f32_e32 v22, v12, v16
	v_mul_f32_e32 v23, v12, v17
	v_lshlrev_b32_e32 v16, 16, v61
	v_and_b32_e32 v17, 0xffff0000, v61
	v_fmac_f32_e32 v22, v13, v16
	v_fmac_f32_e32 v23, v13, v17
	v_lshlrev_b32_e32 v16, 16, v193
	v_and_b32_e32 v17, 0xffff0000, v193
	v_fmac_f32_e32 v22, v14, v16
	v_fmac_f32_e32 v23, v14, v17
	v_lshlrev_b32_e32 v16, 16, v197
	v_and_b32_e32 v17, 0xffff0000, v197
	v_fmac_f32_e32 v22, v15, v16
	v_fmac_f32_e32 v23, v15, v17
	v_lshlrev_b32_e32 v16, 16, v58
	v_and_b32_e32 v17, 0xffff0000, v58
	v_mul_f32_e32 v24, v12, v16
	v_mul_f32_e32 v25, v12, v17
	v_lshlrev_b32_e32 v16, 16, v62
	v_and_b32_e32 v17, 0xffff0000, v62
	v_fmac_f32_e32 v24, v13, v16
	v_fmac_f32_e32 v25, v13, v17
	v_lshlrev_b32_e32 v16, 16, v194
	v_and_b32_e32 v17, 0xffff0000, v194
	v_fmac_f32_e32 v24, v14, v16
	v_fmac_f32_e32 v25, v14, v17
	v_lshlrev_b32_e32 v16, 16, v198
	v_and_b32_e32 v17, 0xffff0000, v198
	v_fmac_f32_e32 v24, v15, v16
	v_fmac_f32_e32 v25, v15, v17
	v_lshlrev_b32_e32 v16, 16, v59
	v_and_b32_e32 v17, 0xffff0000, v59
	v_mul_f32_e32 v26, v12, v16
	v_mul_f32_e32 v27, v12, v17
	v_lshlrev_b32_e32 v16, 16, v63
	v_and_b32_e32 v17, 0xffff0000, v63
	v_fmac_f32_e32 v26, v13, v16
	v_fmac_f32_e32 v27, v13, v17
	v_lshlrev_b32_e32 v16, 16, v195
	v_and_b32_e32 v17, 0xffff0000, v195
	v_fmac_f32_e32 v26, v14, v16
	v_fmac_f32_e32 v27, v14, v17
	v_lshlrev_b32_e32 v16, 16, v199
	v_and_b32_e32 v17, 0xffff0000, v199
	v_fmac_f32_e32 v26, v15, v16
	v_fmac_f32_e32 v27, v15, v17
	v_mov_b32_e32 v18, 0
	v_mov_b32_e32 v19, 0
	v_lshlrev_b32_e32 v11, 3, v191
	v_cvt_pk_fp8_f32 v18, v20, v21
	v_cvt_pk_fp8_f32 v19, v24, v25
	s_nop 0
	v_cvt_pk_fp8_f32 v18, v22, v23 op_sel:[0,0,1]
	v_cvt_pk_fp8_f32 v19, v26, v27 op_sel:[0,0,1]
	s_nop 0
	global_store_dwordx2 v11, v[18:19], s[16:17] sc0 sc1
	v_add_u32_e32 v2, s48, v2
	s_add_u32 s49, s49, s48
	v_min_u32_e32 v190, s43, v2
	v_lshrrev_b32_e32 v9, 3, v190
	v_bfe_u32 v8, v190, 15, 5
	v_and_b32_e32 v10, 7, v190
	v_lshlrev_b32_e32 v11, 9, v9
	v_lshlrev_b32_e32 v9, 4, v9
	v_lshl_add_u32 v10, v10, 4, v11
	global_load_dwordx4 v[32:35], v9, s[14:15]
	global_load_dwordx4 v[48:51], v10, s[44:45] offset:384
	v_cmp_lt_u32_e32 vcc, 0, v8
	s_nop 1
	v_cndmask_b32_e32 v11, v150, v148, vcc
	v_add_u32_e32 v11, v11, v10
	global_load_dwordx4 v[36:39], v11, s[44:45]
	v_cmp_lt_u32_e32 vcc, 1, v8
	s_nop 1
	v_cndmask_b32_e32 v11, v150, v64, vcc
	v_add_u32_e32 v11, v11, v10
	global_load_dwordx4 v[40:43], v11, s[44:45]
	v_cmp_lt_u32_e32 vcc, 2, v8
	s_nop 1
	v_cndmask_b32_e32 v11, v150, v65, vcc
	v_add_u32_e32 v11, v11, v10
	global_load_dwordx4 v[44:47], v11, s[44:45]
	v_add_u32_e32 v191, s42, v2
	v_min_u32_e32 v191, s43, v191
	v_lshrrev_b32_e32 v9, 3, v191
	v_bfe_u32 v8, v191, 15, 5
	v_and_b32_e32 v10, 7, v191
	v_lshlrev_b32_e32 v11, 9, v9
	v_lshlrev_b32_e32 v9, 4, v9
	v_lshl_add_u32 v10, v10, 4, v11
	global_load_dwordx4 v[52:55], v9, s[14:15]
	global_load_dwordx4 v[196:199], v10, s[44:45] offset:384
	v_cmp_lt_u32_e32 vcc, 0, v8
	s_nop 1
	v_cndmask_b32_e32 v11, v150, v148, vcc
	v_add_u32_e32 v11, v11, v10
	global_load_dwordx4 v[56:59], v11, s[44:45]
	v_cmp_lt_u32_e32 vcc, 1, v8
	s_nop 1
	v_cndmask_b32_e32 v11, v150, v64, vcc
	v_add_u32_e32 v11, v11, v10
	global_load_dwordx4 v[60:63], v11, s[44:45]
	v_cmp_lt_u32_e32 vcc, 2, v8
	s_nop 1
	v_cndmask_b32_e32 v11, v150, v65, vcc
	v_add_u32_e32 v11, v11, v10
	global_load_dwordx4 v[192:195], v11, s[44:45]
	s_waitcnt vmcnt(12)
	v_bfe_u32 v8, v238, 15, 5
	v_cmp_lt_u32_e32 vcc, 0, v8
	s_nop 1
	v_cndmask_b32_e32 v200, v149, v200, vcc
	v_cmp_lt_u32_e32 vcc, 1, v8
	s_nop 1
	v_cndmask_b32_e32 v201, v149, v201, vcc
	v_cmp_lt_u32_e32 vcc, 2, v8
	s_nop 1
	v_cndmask_b32_e32 v202, v149, v202, vcc
	v_max3_f32 v9, v200, v201, v202
	v_max_f32_e32 v9, v9, v203
	v_sub_f32_e32 v10, v200, v9
	v_mul_f32_e32 v16, 0x3fb8aa3b, v10
	v_fma_f32 v17, v10, s94, -v16
	v_rndne_f32_e32 v18, v16
	v_fmac_f32_e32 v17, 0x32a5705f, v10
	v_sub_f32_e32 v16, v16, v18
	v_add_f32_e32 v16, v16, v17
	v_exp_f32_e32 v12, v16
	v_cvt_i32_f32_e32 v18, v18
	v_cmp_ngt_f32_e32 vcc, s95, v10
	v_ldexp_f32 v12, v12, v18
	s_nop 1
	v_cndmask_b32_e32 v12, 0, v12, vcc
	v_cmp_nlt_f32_e32 vcc, s96, v10
	s_nop 1
	v_cndmask_b32_e32 v12, v227, v12, vcc
	v_sub_f32_e32 v10, v201, v9
	v_mul_f32_e32 v16, 0x3fb8aa3b, v10
	v_fma_f32 v17, v10, s94, -v16
	v_rndne_f32_e32 v18, v16
	v_fmac_f32_e32 v17, 0x32a5705f, v10
	v_sub_f32_e32 v16, v16, v18
	v_add_f32_e32 v16, v16, v17
	v_exp_f32_e32 v13, v16
	v_cvt_i32_f32_e32 v18, v18
	v_cmp_ngt_f32_e32 vcc, s95, v10
	v_ldexp_f32 v13, v13, v18
	s_nop 1
	v_cndmask_b32_e32 v13, 0, v13, vcc
	v_cmp_nlt_f32_e32 vcc, s96, v10
	s_nop 1
	v_cndmask_b32_e32 v13, v227, v13, vcc
	v_sub_f32_e32 v10, v202, v9
	v_mul_f32_e32 v16, 0x3fb8aa3b, v10
	v_fma_f32 v17, v10, s94, -v16
	v_rndne_f32_e32 v18, v16
	v_fmac_f32_e32 v17, 0x32a5705f, v10
	v_sub_f32_e32 v16, v16, v18
	v_add_f32_e32 v16, v16, v17
	v_exp_f32_e32 v14, v16
	v_cvt_i32_f32_e32 v18, v18
	v_cmp_ngt_f32_e32 vcc, s95, v10
	v_ldexp_f32 v14, v14, v18
	s_nop 1
	v_cndmask_b32_e32 v14, 0, v14, vcc
	v_cmp_nlt_f32_e32 vcc, s96, v10
	s_nop 1
	v_cndmask_b32_e32 v14, v227, v14, vcc
	v_sub_f32_e32 v10, v203, v9
	v_mul_f32_e32 v16, 0x3fb8aa3b, v10
	v_fma_f32 v17, v10, s94, -v16
	v_rndne_f32_e32 v18, v16
	v_fmac_f32_e32 v17, 0x32a5705f, v10
	v_sub_f32_e32 v16, v16, v18
	v_add_f32_e32 v16, v16, v17
	v_exp_f32_e32 v15, v16
	v_cvt_i32_f32_e32 v18, v18
	v_cmp_ngt_f32_e32 vcc, s95, v10
	v_ldexp_f32 v15, v15, v18
	s_nop 1
	v_cndmask_b32_e32 v15, 0, v15, vcc
	v_cmp_nlt_f32_e32 vcc, s96, v10
	s_nop 1
	v_cndmask_b32_e32 v15, v227, v15, vcc
	v_add_f32_e32 v16, v12, v13
	v_add_f32_e32 v16, v14, v16
	v_add_f32_e32 v16, v15, v16
	v_div_scale_f32 v17, s[2:3], v16, v16, 1.0
	v_rcp_f32_e32 v18, v17
	s_nop 0
	v_fma_f32 v19, -v17, v18, 1.0
	v_fmac_f32_e32 v18, v19, v18
	v_div_scale_f32 v20, vcc, 1.0, v16, 1.0
	v_mul_f32_e32 v21, v20, v18
	v_fma_f32 v22, -v17, v21, v20
	v_fmac_f32_e32 v21, v22, v18
	v_fma_f32 v17, -v17, v21, v20
	v_div_fmas_f32 v17, v17, v18, v21
	v_div_fixup_f32 v16, v17, v16, 1.0
	v_mul_f32_e32 v16, 0x41800000, v16
	v_mul_f32_e32 v12, v12, v16
	v_mul_f32_e32 v13, v13, v16
	v_mul_f32_e32 v14, v14, v16
	v_mul_f32_e32 v15, v15, v16
	v_lshlrev_b32_e32 v16, 16, v204
	v_and_b32_e32 v17, 0xffff0000, v204
	v_mul_f32_e32 v20, v12, v16
	v_mul_f32_e32 v21, v12, v17
	v_lshlrev_b32_e32 v16, 16, v208
	v_and_b32_e32 v17, 0xffff0000, v208
	v_fmac_f32_e32 v20, v13, v16
	v_fmac_f32_e32 v21, v13, v17
	v_lshlrev_b32_e32 v16, 16, v212
	v_and_b32_e32 v17, 0xffff0000, v212
	v_fmac_f32_e32 v20, v14, v16
	v_fmac_f32_e32 v21, v14, v17
	v_lshlrev_b32_e32 v16, 16, v216
	v_and_b32_e32 v17, 0xffff0000, v216
	v_fmac_f32_e32 v20, v15, v16
	v_fmac_f32_e32 v21, v15, v17
	v_lshlrev_b32_e32 v16, 16, v205
	v_and_b32_e32 v17, 0xffff0000, v205
	v_mul_f32_e32 v22, v12, v16
	v_mul_f32_e32 v23, v12, v17
	v_lshlrev_b32_e32 v16, 16, v209
	v_and_b32_e32 v17, 0xffff0000, v209
	v_fmac_f32_e32 v22, v13, v16
	v_fmac_f32_e32 v23, v13, v17
	v_lshlrev_b32_e32 v16, 16, v213
	v_and_b32_e32 v17, 0xffff0000, v213
	v_fmac_f32_e32 v22, v14, v16
	v_fmac_f32_e32 v23, v14, v17
	v_lshlrev_b32_e32 v16, 16, v217
	v_and_b32_e32 v17, 0xffff0000, v217
	v_fmac_f32_e32 v22, v15, v16
	v_fmac_f32_e32 v23, v15, v17
	v_lshlrev_b32_e32 v16, 16, v206
	v_and_b32_e32 v17, 0xffff0000, v206
	v_mul_f32_e32 v24, v12, v16
	v_mul_f32_e32 v25, v12, v17
	v_lshlrev_b32_e32 v16, 16, v210
	v_and_b32_e32 v17, 0xffff0000, v210
	v_fmac_f32_e32 v24, v13, v16
	v_fmac_f32_e32 v25, v13, v17
	v_lshlrev_b32_e32 v16, 16, v214
	v_and_b32_e32 v17, 0xffff0000, v214
	v_fmac_f32_e32 v24, v14, v16
	v_fmac_f32_e32 v25, v14, v17
	v_lshlrev_b32_e32 v16, 16, v218
	v_and_b32_e32 v17, 0xffff0000, v218
	v_fmac_f32_e32 v24, v15, v16
	v_fmac_f32_e32 v25, v15, v17
	v_lshlrev_b32_e32 v16, 16, v207
	v_and_b32_e32 v17, 0xffff0000, v207
	v_mul_f32_e32 v26, v12, v16
	v_mul_f32_e32 v27, v12, v17
	v_lshlrev_b32_e32 v16, 16, v211
	v_and_b32_e32 v17, 0xffff0000, v211
	v_fmac_f32_e32 v26, v13, v16
	v_fmac_f32_e32 v27, v13, v17
	v_lshlrev_b32_e32 v16, 16, v215
	v_and_b32_e32 v17, 0xffff0000, v215
	v_fmac_f32_e32 v26, v14, v16
	v_fmac_f32_e32 v27, v14, v17
	v_lshlrev_b32_e32 v16, 16, v219
	v_and_b32_e32 v17, 0xffff0000, v219
	v_fmac_f32_e32 v26, v15, v16
	v_fmac_f32_e32 v27, v15, v17
	v_mov_b32_e32 v18, 0
	v_mov_b32_e32 v19, 0
	v_lshlrev_b32_e32 v11, 3, v238
	v_cvt_pk_fp8_f32 v18, v20, v21
	v_cvt_pk_fp8_f32 v19, v24, v25
	s_nop 0
	v_cvt_pk_fp8_f32 v18, v22, v23 op_sel:[0,0,1]
	v_cvt_pk_fp8_f32 v19, v26, v27 op_sel:[0,0,1]
	s_nop 0
	global_store_dwordx2 v11, v[18:19], s[16:17] sc0 sc1
	v_bfe_u32 v8, v239, 15, 5
	v_cmp_lt_u32_e32 vcc, 0, v8
	s_nop 1
	v_cndmask_b32_e32 v240, v149, v240, vcc
	v_cmp_lt_u32_e32 vcc, 1, v8
	s_nop 1
	v_cndmask_b32_e32 v241, v149, v241, vcc
	v_cmp_lt_u32_e32 vcc, 2, v8
	s_nop 1
	v_cndmask_b32_e32 v242, v149, v242, vcc
	v_max3_f32 v9, v240, v241, v242
	v_max_f32_e32 v9, v9, v243
	v_sub_f32_e32 v10, v240, v9
	v_mul_f32_e32 v16, 0x3fb8aa3b, v10
	v_fma_f32 v17, v10, s94, -v16
	v_rndne_f32_e32 v18, v16
	v_fmac_f32_e32 v17, 0x32a5705f, v10
	v_sub_f32_e32 v16, v16, v18
	v_add_f32_e32 v16, v16, v17
	v_exp_f32_e32 v12, v16
	v_cvt_i32_f32_e32 v18, v18
	v_cmp_ngt_f32_e32 vcc, s95, v10
	v_ldexp_f32 v12, v12, v18
	s_nop 1
	v_cndmask_b32_e32 v12, 0, v12, vcc
	v_cmp_nlt_f32_e32 vcc, s96, v10
	s_nop 1
	v_cndmask_b32_e32 v12, v227, v12, vcc
	v_sub_f32_e32 v10, v241, v9
	v_mul_f32_e32 v16, 0x3fb8aa3b, v10
	v_fma_f32 v17, v10, s94, -v16
	v_rndne_f32_e32 v18, v16
	v_fmac_f32_e32 v17, 0x32a5705f, v10
	v_sub_f32_e32 v16, v16, v18
	v_add_f32_e32 v16, v16, v17
	v_exp_f32_e32 v13, v16
	v_cvt_i32_f32_e32 v18, v18
	v_cmp_ngt_f32_e32 vcc, s95, v10
	v_ldexp_f32 v13, v13, v18
	s_nop 1
	v_cndmask_b32_e32 v13, 0, v13, vcc
	v_cmp_nlt_f32_e32 vcc, s96, v10
	s_nop 1
	v_cndmask_b32_e32 v13, v227, v13, vcc
	v_sub_f32_e32 v10, v242, v9
	v_mul_f32_e32 v16, 0x3fb8aa3b, v10
	v_fma_f32 v17, v10, s94, -v16
	v_rndne_f32_e32 v18, v16
	v_fmac_f32_e32 v17, 0x32a5705f, v10
	v_sub_f32_e32 v16, v16, v18
	v_add_f32_e32 v16, v16, v17
	v_exp_f32_e32 v14, v16
	v_cvt_i32_f32_e32 v18, v18
	v_cmp_ngt_f32_e32 vcc, s95, v10
	v_ldexp_f32 v14, v14, v18
	s_nop 1
	v_cndmask_b32_e32 v14, 0, v14, vcc
	v_cmp_nlt_f32_e32 vcc, s96, v10
	s_nop 1
	v_cndmask_b32_e32 v14, v227, v14, vcc
	v_sub_f32_e32 v10, v243, v9
	v_mul_f32_e32 v16, 0x3fb8aa3b, v10
	v_fma_f32 v17, v10, s94, -v16
	v_rndne_f32_e32 v18, v16
	v_fmac_f32_e32 v17, 0x32a5705f, v10
	v_sub_f32_e32 v16, v16, v18
	v_add_f32_e32 v16, v16, v17
	v_exp_f32_e32 v15, v16
	v_cvt_i32_f32_e32 v18, v18
	v_cmp_ngt_f32_e32 vcc, s95, v10
	v_ldexp_f32 v15, v15, v18
	s_nop 1
	v_cndmask_b32_e32 v15, 0, v15, vcc
	v_cmp_nlt_f32_e32 vcc, s96, v10
	s_nop 1
	v_cndmask_b32_e32 v15, v227, v15, vcc
	v_add_f32_e32 v16, v12, v13
	v_add_f32_e32 v16, v14, v16
	v_add_f32_e32 v16, v15, v16
	v_div_scale_f32 v17, s[2:3], v16, v16, 1.0
	v_rcp_f32_e32 v18, v17
	s_nop 0
	v_fma_f32 v19, -v17, v18, 1.0
	v_fmac_f32_e32 v18, v19, v18
	v_div_scale_f32 v20, vcc, 1.0, v16, 1.0
	v_mul_f32_e32 v21, v20, v18
	v_fma_f32 v22, -v17, v21, v20
	v_fmac_f32_e32 v21, v22, v18
	v_fma_f32 v17, -v17, v21, v20
	v_div_fmas_f32 v17, v17, v18, v21
	v_div_fixup_f32 v16, v17, v16, 1.0
	v_mul_f32_e32 v16, 0x41800000, v16
	v_mul_f32_e32 v12, v12, v16
	v_mul_f32_e32 v13, v13, v16
	v_mul_f32_e32 v14, v14, v16
	v_mul_f32_e32 v15, v15, v16
	v_lshlrev_b32_e32 v16, 16, v244
	v_and_b32_e32 v17, 0xffff0000, v244
	v_mul_f32_e32 v20, v12, v16
	v_mul_f32_e32 v21, v12, v17
	v_lshlrev_b32_e32 v16, 16, v248
	v_and_b32_e32 v17, 0xffff0000, v248
	v_fmac_f32_e32 v20, v13, v16
	v_fmac_f32_e32 v21, v13, v17
	v_lshlrev_b32_e32 v16, 16, v124
	v_and_b32_e32 v17, 0xffff0000, v124
	v_fmac_f32_e32 v20, v14, v16
	v_fmac_f32_e32 v21, v14, v17
	v_lshlrev_b32_e32 v16, 16, v136
	v_and_b32_e32 v17, 0xffff0000, v136
	v_fmac_f32_e32 v20, v15, v16
	v_fmac_f32_e32 v21, v15, v17
	v_lshlrev_b32_e32 v16, 16, v245
	v_and_b32_e32 v17, 0xffff0000, v245
	v_mul_f32_e32 v22, v12, v16
	v_mul_f32_e32 v23, v12, v17
	v_lshlrev_b32_e32 v16, 16, v249
	v_and_b32_e32 v17, 0xffff0000, v249
	v_fmac_f32_e32 v22, v13, v16
	v_fmac_f32_e32 v23, v13, v17
	v_lshlrev_b32_e32 v16, 16, v125
	v_and_b32_e32 v17, 0xffff0000, v125
	v_fmac_f32_e32 v22, v14, v16
	v_fmac_f32_e32 v23, v14, v17
	v_lshlrev_b32_e32 v16, 16, v137
	v_and_b32_e32 v17, 0xffff0000, v137
	v_fmac_f32_e32 v22, v15, v16
	v_fmac_f32_e32 v23, v15, v17
	v_lshlrev_b32_e32 v16, 16, v246
	v_and_b32_e32 v17, 0xffff0000, v246
	v_mul_f32_e32 v24, v12, v16
	v_mul_f32_e32 v25, v12, v17
	v_lshlrev_b32_e32 v16, 16, v250
	v_and_b32_e32 v17, 0xffff0000, v250
	v_fmac_f32_e32 v24, v13, v16
	v_fmac_f32_e32 v25, v13, v17
	v_lshlrev_b32_e32 v16, 16, v126
	v_and_b32_e32 v17, 0xffff0000, v126
	v_fmac_f32_e32 v24, v14, v16
	v_fmac_f32_e32 v25, v14, v17
	v_lshlrev_b32_e32 v16, 16, v138
	v_and_b32_e32 v17, 0xffff0000, v138
	v_fmac_f32_e32 v24, v15, v16
	v_fmac_f32_e32 v25, v15, v17
	v_lshlrev_b32_e32 v16, 16, v247
	v_and_b32_e32 v17, 0xffff0000, v247
	v_mul_f32_e32 v26, v12, v16
	v_mul_f32_e32 v27, v12, v17
	v_lshlrev_b32_e32 v16, 16, v251
	v_and_b32_e32 v17, 0xffff0000, v251
	v_fmac_f32_e32 v26, v13, v16
	v_fmac_f32_e32 v27, v13, v17
	v_lshlrev_b32_e32 v16, 16, v127
	v_and_b32_e32 v17, 0xffff0000, v127
	v_fmac_f32_e32 v26, v14, v16
	v_fmac_f32_e32 v27, v14, v17
	v_lshlrev_b32_e32 v16, 16, v139
	v_and_b32_e32 v17, 0xffff0000, v139
	v_fmac_f32_e32 v26, v15, v16
	v_fmac_f32_e32 v27, v15, v17
	v_mov_b32_e32 v18, 0
	v_mov_b32_e32 v19, 0
	v_lshlrev_b32_e32 v11, 3, v239
	v_cvt_pk_fp8_f32 v18, v20, v21
	v_cvt_pk_fp8_f32 v19, v24, v25
	s_nop 0
	v_cvt_pk_fp8_f32 v18, v22, v23 op_sel:[0,0,1]
	v_cvt_pk_fp8_f32 v19, v26, v27 op_sel:[0,0,1]
	s_nop 0
	global_store_dwordx2 v11, v[18:19], s[16:17] sc0 sc1
	s_cmp_le_u32 s49, s43
	s_cbranch_scc1 .Lmbm_loop
